# waves 0-3 only stage their last two passes (second one in their idle partial-O slab) and store them while waiting at barrier 1; waves 4-7 unchanged
# baseline (speedup 1.0000x reference)
.LBB1_13:
	s_waitcnt vmcnt(12)
	v_cvt_pk_f16_f32 v151, v120, v121
	v_cvt_pk_f16_f32 v150, v100, v101
	v_cvt_pk_f16_f32 v149, v98, v99
	v_cvt_pk_f16_f32 v148, v112, v113
	s_add_i32 s24, s57, 1
	s_cmp_lg_u32 s57, 7
	s_waitcnt vmcnt(11)
	v_mfma_f32_32x32x16_f16 v[0:15], v[144:147], v[148:151], v[0:15]
	s_cselect_b32 s59, s24, 7
	s_lshl_b32 s25, s59, 2
	s_and_b32 s25, s25, 56
	s_or_b32 s58, s25, s27
	s_lshl_b32 s25, s55, 5
	s_and_b32 s59, s59, 1
	s_waitcnt vmcnt(10)
	v_mfma_f32_32x32x16_f16 v[16:31], v[140:143], v[148:151], v[16:31]
	v_cvt_pk_f16_f32 v143, v180, v181
	v_cvt_pk_f16_f32 v142, v124, v125
	v_cvt_pk_f16_f32 v141, v122, v123
	v_cvt_pk_f16_f32 v140, v102, v103
	s_waitcnt vmcnt(9)
	s_nop 0
	v_mfma_f32_32x32x16_f16 v[0:15], v[136:139], v[140:143], v[0:15]
	s_waitcnt vmcnt(8)
	v_mfma_f32_32x32x16_f16 v[16:31], v[132:135], v[140:143], v[16:31]
	s_add_i32 s61, s35, s60
	s_and_b32 s61, s61, 0x3f000
	v_or_b32_e32 v144, s61, v248
	s_add_i32 s61, s36, s60
	s_and_b32 s61, s61, 0x3f000
	v_or_b32_e32 v160, s61, v248
	global_load_dwordx4 v[132:135], v144, s[16:17]
	global_load_dwordx4 v[136:139], v144, s[16:17] offset:1024
	global_load_dwordx4 v[140:143], v144, s[16:17] offset:2048
	s_nop 0
	global_load_dwordx4 v[144:147], v144, s[16:17] offset:3072
	s_nop 0
	global_load_dwordx4 v[148:151], v160, s[16:17]
	global_load_dwordx4 v[152:155], v160, s[16:17] offset:1024
	global_load_dwordx4 v[156:159], v160, s[16:17] offset:2048
	s_nop 0
	global_load_dwordx4 v[160:163], v160, s[16:17] offset:3072
	v_cvt_pk_f16_f32 v253, v96, v97
	v_cvt_pk_f16_f32 v252, v84, v85
	v_cvt_pk_f16_f32 v251, v82, v83
	v_cvt_pk_f16_f32 v250, v80, v81
	s_waitcnt vmcnt(15)
	s_nop 0
	v_mfma_f32_32x32x16_f16 v[0:15], v[60:63], v[250:253], v[0:15]
	s_waitcnt vmcnt(14)
	v_mfma_f32_32x32x16_f16 v[16:31], v[56:59], v[250:253], v[16:31]
	v_cvt_pk_f16_f32 v59, v94, v95
	v_cvt_pk_f16_f32 v58, v90, v91
	v_cvt_pk_f16_f32 v57, v88, v89
	v_cvt_pk_f16_f32 v56, v86, v87
	s_waitcnt vmcnt(13)
	s_nop 0
	v_mfma_f32_32x32x16_f16 v[0:15], v[52:55], v[56:59], v[0:15]
	s_waitcnt vmcnt(12)
	v_mfma_f32_32x32x16_f16 v[16:31], v[48:51], v[56:59], v[16:31]
	v_cvt_pk_f16_f32 v51, v176, v177
	v_cvt_pk_f16_f32 v50, v110, v111
	v_cvt_pk_f16_f32 v49, v108, v109
	v_cvt_pk_f16_f32 v48, v92, v93
	s_waitcnt vmcnt(11)
	s_nop 0
	v_mfma_f32_32x32x16_f16 v[0:15], v[44:47], v[48:51], v[0:15]
	s_waitcnt vmcnt(10)
	v_mfma_f32_32x32x16_f16 v[16:31], v[40:43], v[48:51], v[16:31]
	v_cvt_pk_f16_f32 v43, v206, v207
	v_cvt_pk_f16_f32 v42, v194, v195
	v_cvt_pk_f16_f32 v41, v192, v193
	v_cvt_pk_f16_f32 v40, v174, v175
	s_waitcnt vmcnt(9)
	s_nop 0
	v_mfma_f32_32x32x16_f16 v[0:15], v[36:39], v[40:43], v[0:15]
	s_waitcnt vmcnt(8)
	v_mfma_f32_32x32x16_f16 v[16:31], v[32:35], v[40:43], v[16:31]
	s_add_i32 s61, s37, s60
	s_add_i32 s60, s38, s60
	s_and_b32 s61, s61, 0x3f000
	s_and_b32 s60, s60, 0x3f000
	v_or_b32_e32 v44, s61, v248
	v_or_b32_e32 v60, s60, v248
	global_load_dwordx4 v[32:35], v44, s[16:17]
	global_load_dwordx4 v[36:39], v44, s[16:17] offset:1024
	global_load_dwordx4 v[40:43], v44, s[16:17] offset:2048
	s_nop 0
	global_load_dwordx4 v[44:47], v44, s[16:17] offset:3072
	s_nop 0
	global_load_dwordx4 v[48:51], v60, s[16:17]
	global_load_dwordx4 v[52:55], v60, s[16:17] offset:1024
	global_load_dwordx4 v[56:59], v60, s[16:17] offset:2048
	s_nop 0
	global_load_dwordx4 v[60:63], v60, s[16:17] offset:3072
	v_cvt_pk_f16_f32 v251, v74, v75
	v_cvt_pk_f16_f32 v250, v68, v69
	v_cvt_pk_f16_f32 v249, v66, v67
	v_cvt_pk_f16_f32 v248, v64, v65
	s_waitcnt vmcnt(15)
	s_nop 0
	v_mfma_f32_32x32x16_f16 v[0:15], v[132:135], v[248:251], v[0:15]
	v_cvt_pk_f16_f32 v135, v172, v173
	v_cvt_pk_f16_f32 v134, v106, v107
	v_cvt_pk_f16_f32 v133, v104, v105
	v_cvt_pk_f16_f32 v132, v72, v73
	s_waitcnt vmcnt(14)
	v_mfma_f32_32x32x16_f16 v[16:31], v[136:139], v[248:251], v[16:31]
	s_waitcnt vmcnt(13)
	v_mfma_f32_32x32x16_f16 v[0:15], v[140:143], v[132:135], v[0:15]
	s_waitcnt vmcnt(12)
	v_mfma_f32_32x32x16_f16 v[16:31], v[144:147], v[132:135], v[16:31]
	v_cvt_pk_f16_f32 v135, v202, v203
	v_cvt_pk_f16_f32 v134, v190, v191
	v_cvt_pk_f16_f32 v133, v188, v189
	v_cvt_pk_f16_f32 v132, v170, v171
	s_waitcnt vmcnt(11)
	s_nop 0
	v_mfma_f32_32x32x16_f16 v[0:15], v[148:151], v[132:135], v[0:15]
	s_waitcnt vmcnt(10)
	v_mfma_f32_32x32x16_f16 v[16:31], v[152:155], v[132:135], v[16:31]
	v_cvt_pk_f16_f32 v135, v222, v223
	v_cvt_pk_f16_f32 v134, v216, v217
	v_cvt_pk_f16_f32 v133, v214, v215
	v_cvt_pk_f16_f32 v132, v200, v201
	s_waitcnt vmcnt(9)
	s_nop 0
	v_mfma_f32_32x32x16_f16 v[0:15], v[156:159], v[132:135], v[0:15]
	s_waitcnt vmcnt(8)
	v_mfma_f32_32x32x16_f16 v[16:31], v[160:163], v[132:135], v[16:31]
	v_cvt_pk_f16_f32 v135, v168, v169
	v_cvt_pk_f16_f32 v134, v78, v79
	v_cvt_pk_f16_f32 v133, v76, v77
	v_cvt_pk_f16_f32 v132, v70, v71
	s_waitcnt vmcnt(7)
	s_nop 0
	v_mfma_f32_32x32x16_f16 v[0:15], v[32:35], v[132:135], v[0:15]
	v_cvt_pk_f16_f32 v35, v198, v199
	v_cvt_pk_f16_f32 v34, v186, v187
	v_cvt_pk_f16_f32 v33, v184, v185
	v_cvt_pk_f16_f32 v32, v126, v127
	s_waitcnt vmcnt(6)
	v_mfma_f32_32x32x16_f16 v[16:31], v[36:39], v[132:135], v[16:31]
	s_waitcnt vmcnt(5)
	v_mfma_f32_32x32x16_f16 v[0:15], v[40:43], v[32:35], v[0:15]
	s_waitcnt vmcnt(4)
	v_mfma_f32_32x32x16_f16 v[16:31], v[44:47], v[32:35], v[16:31]
	v_cvt_pk_f16_f32 v35, v220, v221
	v_cvt_pk_f16_f32 v34, v212, v213
	v_cvt_pk_f16_f32 v33, v210, v211
	v_cvt_pk_f16_f32 v32, v196, v197
	s_waitcnt vmcnt(3)
	s_nop 0
	v_mfma_f32_32x32x16_f16 v[0:15], v[48:51], v[32:35], v[0:15]
	s_waitcnt vmcnt(2)
	v_mfma_f32_32x32x16_f16 v[16:31], v[52:55], v[32:35], v[16:31]
	v_cvt_pk_f16_f32 v35, v228, v229
	v_cvt_pk_f16_f32 v34, v226, v227
	v_cvt_pk_f16_f32 v33, v224, v225
	v_cvt_pk_f16_f32 v32, v218, v219
	s_waitcnt vmcnt(1)
	s_nop 0
	v_mfma_f32_32x32x16_f16 v[0:15], v[56:59], v[32:35], v[0:15]
	s_waitcnt vmcnt(0)
	v_mfma_f32_32x32x16_f16 v[16:31], v[60:63], v[32:35], v[16:31]
	s_cmp_lt_u32 s31, 0x200
	s_cbranch_scc0 .Lka_late
	s_or_b32 s62, s39, s59
	s_lshl_b32 s62, s62, 12
	s_lshl_b32 s66, s58, 18
	s_and_b32 s63, s62, 0x3f000
	s_or_b32 s63, s63, s66
	v_or_b32_e32 v252, s63, v231
	global_load_dwordx4 v[48:51], v252, s[6:7]
	global_load_dwordx4 v[52:55], v252, s[6:7] offset:1024
	global_load_dwordx4 v[56:59], v252, s[6:7] offset:2048
	global_load_dwordx4 v[60:63], v252, s[6:7] offset:3072
	s_add_i32 s63, s62, 0x4000
	s_and_b32 s63, s63, 0x3f000
	s_or_b32 s63, s63, s66
	v_or_b32_e32 v253, s63, v231
	global_load_dwordx4 v[40:43], v253, s[6:7] offset:2048
	global_load_dwordx4 v[44:47], v253, s[6:7] offset:3072
	s_add_i32 s63, s62, 0x6000
	s_and_b32 s63, s63, 0x3f000
	s_or_b32 s63, s63, s66
	v_or_b32_e32 v252, s63, v231
	global_load_dwordx4 v[148:151], v252, s[6:7] offset:3072
	s_add_i32 s63, s62, 0x7000
	s_and_b32 s63, s63, 0x3f000
	s_or_b32 s63, s63, s66
	v_or_b32_e32 v253, s63, v231
	global_load_dwordx4 v[132:135], v253, s[6:7]
	global_load_dwordx4 v[136:139], v253, s[6:7] offset:1024
	global_load_dwordx4 v[140:143], v253, s[6:7] offset:2048
	global_load_dwordx4 v[144:147], v253, s[6:7] offset:3072
	s_add_i32 s63, s62, 0x1000
	s_and_b32 s63, s63, 0x3f000
	s_or_b32 s63, s63, s66
	v_or_b32_e32 v252, s63, v231
	global_load_dwordx4 v[152:155], v252, s[6:7]
	global_load_dwordx4 v[156:159], v252, s[6:7] offset:1024
	s_cmp_eq_u32 s12, 0
	s_cbranch_scc1 .Lduty_done
	v_or_b32_e32 v252, s73, v239
	v_lshl_or_b32 v252, v252, 13, v240
	v_add_lshl_u32 v253, v241, s72, 7
	v_add_u32_e32 v253, 0x200, v253
	v_and_or_b32 v252, v253, s54, v252
	v_subrev_u32_e32 v160, 0x13200, v246
	ds_read_b128 v[32:35], v160
	ds_read_b128 v[36:39], v160 offset:1088
	s_waitcnt lgkmcnt(1)
	global_store_dwordx4 v252, v[32:35], s[10:11] nt
	s_nop 0
	ds_read_b128 v[32:35], v160 offset:2176
	v_or_b32_e32 v253, 0x8000, v252
	s_waitcnt lgkmcnt(1)
	global_store_dwordx4 v253, v[36:39], s[10:11] nt
	s_nop 0
	ds_read_b128 v[36:39], v160 offset:3264
	v_or_b32_e32 v253, 0x10000, v252
	s_waitcnt lgkmcnt(1)
	global_store_dwordx4 v253, v[32:35], s[10:11] nt
	s_nop 0
	ds_read_b128 v[32:35], v160 offset:4352
	v_or_b32_e32 v253, 0x18000, v252
	s_waitcnt lgkmcnt(1)
	global_store_dwordx4 v253, v[36:39], s[10:11] nt
	s_nop 0
	ds_read_b128 v[36:39], v160 offset:5440
	v_or_b32_e32 v253, 0x20000, v252
	s_waitcnt lgkmcnt(1)
	global_store_dwordx4 v253, v[32:35], s[10:11] nt
	s_nop 0
	ds_read_b128 v[32:35], v160 offset:6528
	v_or_b32_e32 v253, 0x28000, v252
	s_waitcnt lgkmcnt(1)
	global_store_dwordx4 v253, v[36:39], s[10:11] nt
	s_nop 0
	ds_read_b128 v[36:39], v160 offset:7616
	v_or_b32_e32 v253, 0x30000, v252
	s_waitcnt lgkmcnt(1)
	global_store_dwordx4 v253, v[32:35], s[10:11] nt
	v_or_b32_e32 v253, 0x38000, v252
	s_waitcnt lgkmcnt(0)
	global_store_dwordx4 v253, v[36:39], s[10:11] nt
	v_or_b32_e32 v252, s73, v239
	v_lshl_or_b32 v252, v252, 13, v240
	v_add_lshl_u32 v253, v241, s72, 7
	v_add_u32_e32 v253, 0x300, v253
	v_and_or_b32 v252, v253, s54, v252
	ds_read_b128 v[32:35], v246
	ds_read_b128 v[36:39], v246 offset:1088
	s_waitcnt lgkmcnt(1)
	global_store_dwordx4 v252, v[32:35], s[10:11] nt
	s_nop 0
	ds_read_b128 v[32:35], v246 offset:2176
	v_or_b32_e32 v253, 0x8000, v252
	s_waitcnt lgkmcnt(1)
	global_store_dwordx4 v253, v[36:39], s[10:11] nt
	s_nop 0
	ds_read_b128 v[36:39], v246 offset:3264
	v_or_b32_e32 v253, 0x10000, v252
	s_waitcnt lgkmcnt(1)
	global_store_dwordx4 v253, v[32:35], s[10:11] nt
	s_nop 0
	ds_read_b128 v[32:35], v246 offset:4352
	v_or_b32_e32 v253, 0x18000, v252
	s_waitcnt lgkmcnt(1)
	global_store_dwordx4 v253, v[36:39], s[10:11] nt
	s_nop 0
	ds_read_b128 v[36:39], v246 offset:5440
	v_or_b32_e32 v253, 0x20000, v252
	s_waitcnt lgkmcnt(1)
	global_store_dwordx4 v253, v[32:35], s[10:11] nt
	s_nop 0
	ds_read_b128 v[32:35], v246 offset:6528
	v_or_b32_e32 v253, 0x28000, v252
	s_waitcnt lgkmcnt(1)
	global_store_dwordx4 v253, v[36:39], s[10:11] nt
	s_nop 0
	ds_read_b128 v[36:39], v246 offset:7616
	v_or_b32_e32 v253, 0x30000, v252
	s_waitcnt lgkmcnt(1)
	global_store_dwordx4 v253, v[32:35], s[10:11] nt
	v_or_b32_e32 v253, 0x38000, v252
	s_waitcnt lgkmcnt(0)
	global_store_dwordx4 v253, v[36:39], s[10:11] nt

.Lka_done:
	ds_read2_b32 v[0:1], v235 offset1:32
	ds_read2_b32 v[2:3], v235 offset0:64 offset1:96
	ds_read2_b32 v[4:5], v235 offset0:128 offset1:160
	ds_read2_b32 v[6:7], v235 offset0:192 offset1:224
	ds_read2_b32 v[10:11], v236 offset0:128 offset1:160
	ds_read2_b32 v[16:17], v165 offset1:32
	ds_write_b128 v232, v[128:131]
	s_waitcnt lgkmcnt(6)
	v_max_f32_e32 v8, v1, v1
	v_max_f32_e32 v9, v0, v0
	v_max_f32_e32 v8, v9, v8
	s_waitcnt lgkmcnt(5)
	v_max3_f32 v8, v8, v2, v3
	s_waitcnt lgkmcnt(4)
	v_max3_f32 v8, v8, v4, v5
	s_waitcnt lgkmcnt(3)
	v_max3_f32 v14, v8, v6, v7
	ds_read2_b32 v[8:9], v236 offset1:32
	v_sub_f32_e32 v0, v0, v14
	v_sub_f32_e32 v1, v1, v14
	v_exp_f32_e32 v0, v0
	v_exp_f32_e32 v1, v1
	v_sub_f32_e32 v4, v4, v14
	v_sub_f32_e32 v5, v5, v14
	v_exp_f32_e32 v4, v4
	v_exp_f32_e32 v5, v5
	s_waitcnt lgkmcnt(0)
	v_pk_mul_f32 v[0:1], v[8:9], v[0:1]
	ds_read2_b32 v[8:9], v236 offset0:64 offset1:96
	v_sub_f32_e32 v2, v2, v14
	v_sub_f32_e32 v3, v3, v14
	v_exp_f32_e32 v2, v2
	v_exp_f32_e32 v3, v3
	ds_read2_b32 v[12:13], v236 offset0:192 offset1:224
	v_sub_f32_e32 v6, v6, v14
	v_sub_f32_e32 v7, v7, v14
	v_pk_mul_f32 v[18:19], v[10:11], v[4:5]
	v_sub_f32_e32 v4, v247, v14
	ds_read2_b32 v[22:23], v165 offset0:64 offset1:96
	ds_read2_b32 v[24:25], v165 offset0:128 offset1:160
	ds_read2_b32 v[26:27], v165 offset0:192 offset1:224
	v_exp_f32_e32 v6, v6
	v_exp_f32_e32 v7, v7
	v_exp_f32_e32 v34, v4
	v_max_f32_e32 v4, v17, v17
	v_max_f32_e32 v5, v16, v16
	v_add_f32_e32 v0, 0, v0
	s_waitcnt lgkmcnt(4)
	v_pk_mul_f32 v[2:3], v[8:9], v[2:3]
	v_max_f32_e32 v4, v5, v4
	v_add_f32_e32 v0, v0, v1
	s_waitcnt lgkmcnt(2)
	v_max3_f32 v4, v4, v22, v23
	v_add_f32_e32 v0, v0, v2
	s_waitcnt lgkmcnt(1)
	v_max3_f32 v4, v4, v24, v25
	v_add_f32_e32 v0, v0, v3
	v_pk_mul_f32 v[20:21], v[12:13], v[6:7]
	s_waitcnt lgkmcnt(0)
	v_max3_f32 v35, v4, v26, v27
	v_add_f32_e32 v18, v0, v18
	ds_read_b128 v[0:3], v245
	ds_read_b128 v[4:7], v237
	v_sub_f32_e32 v8, v16, v35
	v_exp_f32_e32 v16, v8
	ds_read2_b32 v[28:29], v242 offset1:32
	ds_read_b128 v[8:11], v245 offset:34816
	ds_read_b128 v[12:15], v245 offset:60928
	s_min_u32 s57, s57, 5
	s_waitcnt lgkmcnt(3)
	v_pk_add_f32 v[0:1], v[0:1], v[4:5]
	v_pk_add_f32 v[2:3], v[2:3], v[6:7]
	v_pk_fma_f32 v[30:31], v[16:17], v[0:1], 0 op_sel_hi:[0,1,0]
	v_sub_f32_e32 v0, v17, v35
	v_pk_fma_f32 v[32:33], v[16:17], v[2:3], 0 op_sel_hi:[0,1,0]
	v_exp_f32_e32 v17, v0
	v_add_f32_e32 v0, v18, v19
	v_add_f32_e32 v0, v0, v20
	v_add_f32_e32 v36, v0, v21
	ds_read_b128 v[0:3], v245 offset:8704
	ds_read_b128 v[4:7], v245 offset:17408
	s_waitcnt lgkmcnt(4)
	v_pk_mul_f32 v[18:19], v[28:29], v[16:17]
	v_sub_f32_e32 v16, v22, v35
	v_exp_f32_e32 v16, v16
	v_add_f32_e32 v20, 0, v18
	v_mov_b32_e32 v18, v17
	s_waitcnt lgkmcnt(1)
	v_pk_fma_f32 v[0:1], v[18:19], v[0:1], v[30:31] op_sel_hi:[0,1,1]
	v_pk_fma_f32 v[2:3], v[18:19], v[2:3], v[32:33] op_sel_hi:[0,1,1]
	s_waitcnt lgkmcnt(0)
	v_pk_fma_f32 v[4:5], v[16:17], v[4:5], v[0:1] op_sel_hi:[0,1,1]
	v_sub_f32_e32 v0, v23, v35
	v_pk_fma_f32 v[6:7], v[16:17], v[6:7], v[2:3] op_sel_hi:[0,1,1]
	v_exp_f32_e32 v17, v0
	v_add_f32_e32 v21, v20, v19
	ds_read_b128 v[0:3], v245 offset:26112
	ds_read2_b32 v[18:19], v242 offset0:64 offset1:96
	v_sub_f32_e32 v22, v24, v35
	v_exp_f32_e32 v22, v22
	v_mov_b32_e32 v20, v17
	s_waitcnt lgkmcnt(1)
	v_pk_fma_f32 v[0:1], v[20:21], v[0:1], v[4:5] op_sel_hi:[0,1,1]
	v_pk_fma_f32 v[2:3], v[20:21], v[2:3], v[6:7] op_sel_hi:[0,1,1]
	ds_read2_b32 v[4:5], v242 offset0:128 offset1:160
	v_pk_fma_f32 v[8:9], v[22:23], v[8:9], v[0:1] op_sel_hi:[0,1,1]
	v_sub_f32_e32 v0, v25, v35
	v_pk_fma_f32 v[10:11], v[22:23], v[10:11], v[2:3] op_sel_hi:[0,1,1]
	v_exp_f32_e32 v23, v0
	s_waitcnt lgkmcnt(1)
	v_pk_mul_f32 v[0:1], v[18:19], v[16:17]
	s_lshl_b32 s58, s58, 18
	v_add_f32_e32 v0, v21, v0
	v_add_f32_e32 v2, v0, v1
	s_waitcnt lgkmcnt(0)
	v_pk_mul_f32 v[0:1], v[4:5], v[22:23]
	v_sub_f32_e32 v4, v26, v35
	v_add_f32_e32 v0, v2, v0
	v_add_f32_e32 v17, v0, v1
	ds_read_b128 v[0:3], v245 offset:43520
	v_exp_f32_e32 v18, v4
	ds_read2_b32 v[20:21], v242 offset0:192 offset1:224
	v_sub_f32_e32 v4, v27, v35
	v_exp_f32_e32 v19, v4
	ds_read_b128 v[4:7], v245 offset:52224
	v_mov_b32_e32 v16, v23
	s_waitcnt lgkmcnt(2)
	v_pk_fma_f32 v[0:1], v[16:17], v[0:1], v[8:9] op_sel_hi:[0,1,1]
	s_waitcnt lgkmcnt(1)
	v_pk_mul_f32 v[8:9], v[20:21], v[18:19]
	v_pk_fma_f32 v[2:3], v[16:17], v[2:3], v[10:11] op_sel_hi:[0,1,1]
	v_add_f32_e32 v8, v17, v8
	v_add_f32_e32 v8, v8, v9
	s_waitcnt lgkmcnt(0)
	v_pk_fma_f32 v[0:1], v[18:19], v[4:5], v[0:1] op_sel_hi:[0,1,1]
	v_div_scale_f32 v5, s[60:61], v8, v8, 1.0
	v_pk_fma_f32 v[2:3], v[18:19], v[6:7], v[2:3] op_sel_hi:[0,1,1]
	v_rcp_f32_e32 v6, v5
	v_mov_b32_e32 v4, v19
	v_pk_fma_f32 v[2:3], v[4:5], v[14:15], v[2:3] op_sel_hi:[0,1,1]
	v_pk_fma_f32 v[0:1], v[4:5], v[12:13], v[0:1] op_sel_hi:[0,1,1]
	v_fma_f32 v4, -v5, v6, 1.0
	v_fmac_f32_e32 v6, v4, v6
	v_div_scale_f32 v4, vcc, 1.0, v8, 1.0
	v_mul_f32_e32 v7, v4, v6
	v_fma_f32 v9, -v5, v7, v4
	v_fmac_f32_e32 v7, v9, v6
	v_fma_f32 v4, -v5, v7, v4
	v_div_fmas_f32 v4, v4, v6, v7
	s_lshl_b32 s60, s56, 19
	s_lshl_b32 s61, s55, 13
	v_div_fixup_f32 v4, v4, v8, 1.0
	s_add_i32 s60, s60, s61
	v_pk_mul_f32 v[2:3], v[2:3], v[4:5] op_sel_hi:[1,0]
	v_pk_mul_f32 v[0:1], v[0:1], v[4:5] op_sel_hi:[1,0]
	v_or_b32_e32 v4, s60, v230
	s_lshl_b32 s60, s57, 2
	s_add_i32 s60, s60, 8
	s_and_b32 s60, s60, 56
	s_and_b32 s57, s57, 1
	s_or_b32 s60, s60, s27
	s_or_b32 s57, s57, s28
	s_lshl_b32 s60, s60, 19
	s_lshl_b32 s57, s57, 13
	s_add_i32 s60, s60, s57
	s_or_b32 s62, s39, s59
	s_lshl_b32 s62, s62, 12
	global_store_dwordx4 v4, v[0:3], s[8:9] nt
	v_mov_b32_e32 v252, v34
	v_mov_b32_e32 v253, v36
	v_or_b32_e32 v0, s60, v230
	s_barrier
	global_load_dwordx4 v[128:131], v0, s[4:5]
	s_add_i32 s63, s62, 0x4000
	s_and_b32 s63, s63, 0x3f000
	s_or_b32 s63, s63, s58
	v_or_b32_e32 v2, s63, v231
	global_load_dwordx4 v[32:35], v2, s[6:7]
	global_load_dwordx4 v[36:39], v2, s[6:7] offset:1024
	s_add_i32 s63, s62, 0x5000
	s_and_b32 s63, s63, 0x3f000
	s_or_b32 s63, s63, s58
	v_or_b32_e32 v3, s63, v231
	global_load_dwordx4 v[16:19], v3, s[6:7]
	global_load_dwordx4 v[20:23], v3, s[6:7] offset:1024
	global_load_dwordx4 v[24:27], v3, s[6:7] offset:2048
	global_load_dwordx4 v[28:31], v3, s[6:7] offset:3072
	s_add_i32 s63, s62, 0x6000
	s_and_b32 s63, s63, 0x3f000
	s_or_b32 s63, s63, s58
	v_or_b32_e32 v2, s63, v231
	global_load_dwordx4 v[4:7], v2, s[6:7]
	global_load_dwordx4 v[8:11], v2, s[6:7] offset:1024
	global_load_dwordx4 v[12:15], v2, s[6:7] offset:2048
	v_div_scale_f32 v1, s[64:65], v253, v253, v252
	v_rcp_f32_e32 v2, v1
	s_nop 0
	v_fma_f32 v0, -v1, v2, 1.0
	v_fmac_f32_e32 v2, v0, v2
	v_div_scale_f32 v0, vcc, v252, v253, v252
	v_mul_f32_e32 v3, v0, v2
	v_fma_f32 v248, -v1, v3, v0
	v_fmac_f32_e32 v3, v248, v2
	v_fma_f32 v0, -v1, v3, v0
	v_div_fmas_f32 v0, v0, v2, v3
	v_div_fixup_f32 v1, v0, v253, v252
	v_mul_f32_e32 v0, s18, v1
	v_mov_b32_e32 v2, s26
	v_mov_b32_e32 v3, s23
	v_cmp_eq_u32_e64 s[64:65], 0, v233
	v_cmp_eq_u32_e64 s[66:67], 1, v233
	v_cmp_eq_u32_e64 s[68:69], 2, v233
	v_cmp_eq_u32_e64 s[70:71], 3, v233
	v_cndmask_b32_e64 v248, v2, v3, s[64:65]
	v_cndmask_b32_e64 v249, v2, v3, s[66:67]
	v_cndmask_b32_e64 v250, v2, v3, s[68:69]
	v_cndmask_b32_e64 v251, v2, v3, s[70:71]
	v_mul_f32_e32 v248, v1, v248
	v_mul_f32_e32 v249, v1, v249
	v_mul_f32_e32 v250, v1, v250
	v_mul_f32_e32 v251, v1, v251
	v_cndmask_b32_e64 v248, v0, v248, s[2:3]
	v_cndmask_b32_e64 v249, v0, v249, s[2:3]
	v_cndmask_b32_e64 v250, v0, v250, s[2:3]
	v_cndmask_b32_e64 v251, v0, v251, s[2:3]
	v_mul_f32_e32 v248, v248, v208
	v_mul_f32_e32 v249, v249, v209
	v_mul_f32_e32 v250, v250, v204
	v_mul_f32_e32 v251, v251, v205
	ds_write_b128 v238, v[248:251]
	v_cmp_eq_u32_e64 s[64:65], 4, v233
	v_cmp_eq_u32_e64 s[66:67], 5, v233
	v_cmp_eq_u32_e64 s[68:69], 6, v233
	v_cmp_eq_u32_e64 s[70:71], 7, v233
	v_cndmask_b32_e64 v248, v2, v3, s[64:65]
	v_cndmask_b32_e64 v249, v2, v3, s[66:67]
	v_cndmask_b32_e64 v250, v2, v3, s[68:69]
	v_cndmask_b32_e64 v251, v2, v3, s[70:71]
	v_mul_f32_e32 v248, v1, v248
	v_mul_f32_e32 v249, v1, v249
	v_mul_f32_e32 v250, v1, v250
	v_mul_f32_e32 v251, v1, v251
	v_cndmask_b32_e64 v248, v0, v248, s[2:3]
	v_cndmask_b32_e64 v249, v0, v249, s[2:3]
	v_cndmask_b32_e64 v250, v0, v250, s[2:3]
	v_cndmask_b32_e64 v251, v0, v251, s[2:3]
	v_mul_f32_e32 v248, v248, v182
	v_mul_f32_e32 v249, v249, v183
	v_mul_f32_e32 v250, v250, v178
	v_mul_f32_e32 v251, v251, v179
	ds_write_b128 v238, v[248:251] offset:32
	v_cmp_eq_u32_e64 s[64:65], 8, v233
	v_cmp_eq_u32_e64 s[66:67], 9, v233
	v_cmp_eq_u32_e64 s[68:69], 10, v233
	v_cmp_eq_u32_e64 s[70:71], 11, v233
	v_cndmask_b32_e64 v248, v2, v3, s[64:65]
	v_cndmask_b32_e64 v249, v2, v3, s[66:67]
	v_cndmask_b32_e64 v250, v2, v3, s[68:69]
	v_cndmask_b32_e64 v251, v2, v3, s[70:71]
	v_mul_f32_e32 v248, v1, v248
	v_mul_f32_e32 v249, v1, v249
	v_mul_f32_e32 v250, v1, v250
	v_mul_f32_e32 v251, v1, v251
	v_cndmask_b32_e64 v248, v0, v248, s[2:3]
	v_cndmask_b32_e64 v249, v0, v249, s[2:3]
	v_cndmask_b32_e64 v250, v0, v250, s[2:3]
	v_cndmask_b32_e64 v251, v0, v251, s[2:3]
	v_mul_f32_e32 v248, v248, v166
	v_mul_f32_e32 v249, v249, v167
	v_mul_f32_e32 v250, v250, v118
	v_mul_f32_e32 v251, v251, v119
	ds_write_b128 v238, v[248:251] offset:64
	v_cmp_eq_u32_e64 s[64:65], 12, v233
	v_cmp_eq_u32_e64 s[66:67], 13, v233
	v_cmp_eq_u32_e64 s[68:69], 14, v233
	v_cmp_eq_u32_e64 s[70:71], 15, v233
	v_cndmask_b32_e64 v248, v2, v3, s[64:65]
	v_cndmask_b32_e64 v249, v2, v3, s[66:67]
	v_cndmask_b32_e64 v250, v2, v3, s[68:69]
	v_cndmask_b32_e64 v251, v2, v3, s[70:71]
	v_mul_f32_e32 v248, v1, v248
	v_mul_f32_e32 v249, v1, v249
	v_mul_f32_e32 v250, v1, v250
	v_mul_f32_e32 v251, v1, v251
	v_cndmask_b32_e64 v248, v0, v248, s[2:3]
	v_cndmask_b32_e64 v249, v0, v249, s[2:3]
	v_cndmask_b32_e64 v250, v0, v250, s[2:3]
	v_cndmask_b32_e64 v251, v0, v251, s[2:3]
	v_mul_f32_e32 v248, v248, v116
	v_mul_f32_e32 v249, v249, v117
	v_mul_f32_e32 v250, v250, v114
	v_mul_f32_e32 v251, v251, v115
	ds_write_b128 v238, v[248:251] offset:96
	v_pk_mul_f32 v[248:249], v[0:1], v[112:113] op_sel_hi:[0,1]
	v_pk_mul_f32 v[250:251], v[0:1], v[98:99] op_sel_hi:[0,1]
	ds_write_b128 v238, v[248:251] offset:128
	v_pk_mul_f32 v[248:249], v[0:1], v[100:101] op_sel_hi:[0,1]
	v_pk_mul_f32 v[250:251], v[0:1], v[120:121] op_sel_hi:[0,1]
	ds_write_b128 v238, v[248:251] offset:160
	v_pk_mul_f32 v[248:249], v[0:1], v[102:103] op_sel_hi:[0,1]
	v_pk_mul_f32 v[250:251], v[0:1], v[122:123] op_sel_hi:[0,1]
	ds_write_b128 v238, v[248:251] offset:192
	v_pk_mul_f32 v[248:249], v[0:1], v[124:125] op_sel_hi:[0,1]
	v_pk_mul_f32 v[250:251], v[0:1], v[180:181] op_sel_hi:[0,1]
	ds_write_b128 v238, v[248:251] offset:224
	s_lshl_b32 s56, s56, 11
	s_add_i32 s56, s56, s25
	v_or_b32_e32 v252, s56, v239
	v_add_lshl_u32 v253, v241, s55, 7
	v_lshl_or_b32 v1, v252, 13, v240
	v_and_or_b32 v2, v253, s54, v1
	ds_read_b128 v[248:251], v246
	ds_read_b128 v[160:163], v246 offset:1088
	s_waitcnt lgkmcnt(1)
	global_store_dwordx4 v2, v[248:251], s[10:11] nt
	s_nop 0
	ds_read_b128 v[248:251], v246 offset:2176
	v_or_b32_e32 v3, 0x8000, v2
	s_waitcnt lgkmcnt(1)
	global_store_dwordx4 v3, v[160:163], s[10:11] nt
	s_nop 0
	ds_read_b128 v[160:163], v246 offset:3264
	v_or_b32_e32 v252, 0x10000, v2
	s_waitcnt lgkmcnt(1)
	global_store_dwordx4 v252, v[248:251], s[10:11] nt
	s_nop 0
	ds_read_b128 v[248:251], v246 offset:4352
	v_or_b32_e32 v3, 0x18000, v2
	s_waitcnt lgkmcnt(1)
	global_store_dwordx4 v3, v[160:163], s[10:11] nt
	s_nop 0
	ds_read_b128 v[160:163], v246 offset:5440
	v_or_b32_e32 v252, 0x20000, v2
	s_waitcnt lgkmcnt(1)
	global_store_dwordx4 v252, v[248:251], s[10:11] nt
	s_nop 0
	ds_read_b128 v[248:251], v246 offset:6528
	v_or_b32_e32 v3, 0x28000, v2
	s_waitcnt lgkmcnt(1)
	global_store_dwordx4 v3, v[160:163], s[10:11] nt
	s_nop 0
	ds_read_b128 v[160:163], v246 offset:7616
	v_or_b32_e32 v252, 0x30000, v2
	s_waitcnt lgkmcnt(1)
	global_store_dwordx4 v252, v[248:251], s[10:11] nt
	v_or_b32_e32 v3, 0x38000, v2
	s_waitcnt lgkmcnt(0)
	global_store_dwordx4 v3, v[160:163], s[10:11] nt
	v_pk_mul_f32 v[248:249], v[0:1], v[80:81] op_sel_hi:[0,1]
	v_pk_mul_f32 v[250:251], v[0:1], v[82:83] op_sel_hi:[0,1]
	ds_write_b128 v238, v[248:251]
	v_pk_mul_f32 v[248:249], v[0:1], v[84:85] op_sel_hi:[0,1]
	v_pk_mul_f32 v[250:251], v[0:1], v[96:97] op_sel_hi:[0,1]
	ds_write_b128 v238, v[248:251] offset:32
	v_pk_mul_f32 v[248:249], v[0:1], v[86:87] op_sel_hi:[0,1]
	v_pk_mul_f32 v[250:251], v[0:1], v[88:89] op_sel_hi:[0,1]
	ds_write_b128 v238, v[248:251] offset:64
	v_pk_mul_f32 v[248:249], v[0:1], v[90:91] op_sel_hi:[0,1]
	v_pk_mul_f32 v[250:251], v[0:1], v[94:95] op_sel_hi:[0,1]
	ds_write_b128 v238, v[248:251] offset:96
	v_pk_mul_f32 v[248:249], v[0:1], v[92:93] op_sel_hi:[0,1]
	v_pk_mul_f32 v[250:251], v[0:1], v[108:109] op_sel_hi:[0,1]
	ds_write_b128 v238, v[248:251] offset:128
	v_pk_mul_f32 v[248:249], v[0:1], v[110:111] op_sel_hi:[0,1]
	v_pk_mul_f32 v[250:251], v[0:1], v[176:177] op_sel_hi:[0,1]
	ds_write_b128 v238, v[248:251] offset:160
	v_pk_mul_f32 v[248:249], v[0:1], v[174:175] op_sel_hi:[0,1]
	v_pk_mul_f32 v[250:251], v[0:1], v[192:193] op_sel_hi:[0,1]
	ds_write_b128 v238, v[248:251] offset:192
	v_pk_mul_f32 v[248:249], v[0:1], v[194:195] op_sel_hi:[0,1]
	v_pk_mul_f32 v[250:251], v[0:1], v[206:207] op_sel_hi:[0,1]
	ds_write_b128 v238, v[248:251] offset:224
	v_add_u32_e32 v252, 0x100, v253
	v_and_or_b32 v2, v252, s54, v1
	ds_read_b128 v[248:251], v246
	ds_read_b128 v[160:163], v246 offset:1088
	s_waitcnt lgkmcnt(1)
	global_store_dwordx4 v2, v[248:251], s[10:11] nt
	s_nop 0
	ds_read_b128 v[248:251], v246 offset:2176
	v_or_b32_e32 v3, 0x8000, v2
	s_waitcnt lgkmcnt(1)
	global_store_dwordx4 v3, v[160:163], s[10:11] nt
	s_nop 0
	ds_read_b128 v[160:163], v246 offset:3264
	v_or_b32_e32 v252, 0x10000, v2
	s_waitcnt lgkmcnt(1)
	global_store_dwordx4 v252, v[248:251], s[10:11] nt
	s_nop 0
	ds_read_b128 v[248:251], v246 offset:4352
	v_or_b32_e32 v3, 0x18000, v2
	s_waitcnt lgkmcnt(1)
	global_store_dwordx4 v3, v[160:163], s[10:11] nt
	s_nop 0
	ds_read_b128 v[160:163], v246 offset:5440
	v_or_b32_e32 v252, 0x20000, v2
	s_waitcnt lgkmcnt(1)
	global_store_dwordx4 v252, v[248:251], s[10:11] nt
	s_nop 0
	ds_read_b128 v[248:251], v246 offset:6528
	v_or_b32_e32 v3, 0x28000, v2
	s_waitcnt lgkmcnt(1)
	global_store_dwordx4 v3, v[160:163], s[10:11] nt
	s_nop 0
	ds_read_b128 v[160:163], v246 offset:7616
	v_or_b32_e32 v252, 0x30000, v2
	s_waitcnt lgkmcnt(1)
	global_store_dwordx4 v252, v[248:251], s[10:11] nt
	v_or_b32_e32 v3, 0x38000, v2
	s_waitcnt lgkmcnt(0)
	global_store_dwordx4 v3, v[160:163], s[10:11] nt
	s_add_i32 s63, s62, 0x3000
	s_and_b32 s63, s63, 0x3f000
	s_or_b32 s63, s63, s58
	v_or_b32_e32 v2, s63, v231
	global_load_dwordx4 v[80:83], v2, s[6:7]
	global_load_dwordx4 v[84:87], v2, s[6:7] offset:1024
	global_load_dwordx4 v[88:91], v2, s[6:7] offset:2048
	global_load_dwordx4 v[92:95], v2, s[6:7] offset:3072
	s_add_i32 s63, s62, 0x2000
	s_and_b32 s63, s63, 0x3f000
	s_or_b32 s63, s63, s58
	v_or_b32_e32 v3, s63, v231
	global_load_dwordx4 v[96:99], v3, s[6:7]
	global_load_dwordx4 v[100:103], v3, s[6:7] offset:1024
	global_load_dwordx4 v[108:111], v3, s[6:7] offset:2048
	global_load_dwordx4 v[192:195], v3, s[6:7] offset:3072
	s_add_i32 s63, s62, 0x1000
	s_and_b32 s63, s63, 0x3f000
	s_or_b32 s63, s63, s58
	v_or_b32_e32 v2, s63, v231
	global_load_dwordx4 v[174:177], v2, s[6:7] offset:2048
	global_load_dwordx4 v[178:181], v2, s[6:7] offset:3072
	s_cmp_lt_u32 s31, 0x200
	s_cbranch_scc0 .Lp2_full
	v_subrev_u32_e32 v252, 0x13200, v238
	v_pk_mul_f32 v[248:249], v[0:1], v[64:65] op_sel_hi:[0,1]
	v_pk_mul_f32 v[250:251], v[0:1], v[66:67] op_sel_hi:[0,1]
	ds_write_b128 v252, v[248:251]
	v_pk_mul_f32 v[248:249], v[0:1], v[68:69] op_sel_hi:[0,1]
	v_pk_mul_f32 v[250:251], v[0:1], v[74:75] op_sel_hi:[0,1]
	ds_write_b128 v252, v[248:251] offset:32
	v_pk_mul_f32 v[248:249], v[0:1], v[72:73] op_sel_hi:[0,1]
	v_pk_mul_f32 v[250:251], v[0:1], v[104:105] op_sel_hi:[0,1]
	ds_write_b128 v252, v[248:251] offset:64
	v_pk_mul_f32 v[248:249], v[0:1], v[106:107] op_sel_hi:[0,1]
	v_pk_mul_f32 v[250:251], v[0:1], v[172:173] op_sel_hi:[0,1]
	ds_write_b128 v252, v[248:251] offset:96
	v_pk_mul_f32 v[248:249], v[0:1], v[170:171] op_sel_hi:[0,1]
	v_pk_mul_f32 v[250:251], v[0:1], v[188:189] op_sel_hi:[0,1]
	ds_write_b128 v252, v[248:251] offset:128
	v_pk_mul_f32 v[248:249], v[0:1], v[190:191] op_sel_hi:[0,1]
	v_pk_mul_f32 v[250:251], v[0:1], v[202:203] op_sel_hi:[0,1]
	ds_write_b128 v252, v[248:251] offset:160
	v_pk_mul_f32 v[248:249], v[0:1], v[200:201] op_sel_hi:[0,1]
	v_pk_mul_f32 v[250:251], v[0:1], v[214:215] op_sel_hi:[0,1]
	ds_write_b128 v252, v[248:251] offset:192
	v_pk_mul_f32 v[248:249], v[0:1], v[216:217] op_sel_hi:[0,1]
	v_pk_mul_f32 v[250:251], v[0:1], v[222:223] op_sel_hi:[0,1]
	ds_write_b128 v252, v[248:251] offset:224
	s_branch .Lp2_done
.Lp2_full:
	v_pk_mul_f32 v[248:249], v[0:1], v[64:65] op_sel_hi:[0,1]
	v_pk_mul_f32 v[250:251], v[0:1], v[66:67] op_sel_hi:[0,1]
	ds_write_b128 v238, v[248:251]
	v_pk_mul_f32 v[248:249], v[0:1], v[68:69] op_sel_hi:[0,1]
	v_pk_mul_f32 v[250:251], v[0:1], v[74:75] op_sel_hi:[0,1]
	ds_write_b128 v238, v[248:251] offset:32
	v_pk_mul_f32 v[248:249], v[0:1], v[72:73] op_sel_hi:[0,1]
	v_pk_mul_f32 v[250:251], v[0:1], v[104:105] op_sel_hi:[0,1]
	ds_write_b128 v238, v[248:251] offset:64
	v_pk_mul_f32 v[248:249], v[0:1], v[106:107] op_sel_hi:[0,1]
	v_pk_mul_f32 v[250:251], v[0:1], v[172:173] op_sel_hi:[0,1]
	ds_write_b128 v238, v[248:251] offset:96
	v_pk_mul_f32 v[248:249], v[0:1], v[170:171] op_sel_hi:[0,1]
	v_pk_mul_f32 v[250:251], v[0:1], v[188:189] op_sel_hi:[0,1]
	ds_write_b128 v238, v[248:251] offset:128
	v_pk_mul_f32 v[248:249], v[0:1], v[190:191] op_sel_hi:[0,1]
	v_pk_mul_f32 v[250:251], v[0:1], v[202:203] op_sel_hi:[0,1]
	ds_write_b128 v238, v[248:251] offset:160
	v_pk_mul_f32 v[248:249], v[0:1], v[200:201] op_sel_hi:[0,1]
	v_pk_mul_f32 v[250:251], v[0:1], v[214:215] op_sel_hi:[0,1]
	ds_write_b128 v238, v[248:251] offset:192
	v_pk_mul_f32 v[248:249], v[0:1], v[216:217] op_sel_hi:[0,1]
	v_pk_mul_f32 v[250:251], v[0:1], v[222:223] op_sel_hi:[0,1]
	ds_write_b128 v238, v[248:251] offset:224
	v_add_u32_e32 v252, 0x200, v253
	v_and_or_b32 v2, v252, s54, v1
	ds_read_b128 v[248:251], v246
	ds_read_b128 v[160:163], v246 offset:1088
	s_waitcnt lgkmcnt(1)
	global_store_dwordx4 v2, v[248:251], s[10:11] nt
	s_nop 0
	ds_read_b128 v[248:251], v246 offset:2176
	v_or_b32_e32 v3, 0x8000, v2
	s_waitcnt lgkmcnt(1)
	global_store_dwordx4 v3, v[160:163], s[10:11] nt
	s_nop 0
	ds_read_b128 v[160:163], v246 offset:3264
	v_or_b32_e32 v252, 0x10000, v2
	s_waitcnt lgkmcnt(1)
	global_store_dwordx4 v252, v[248:251], s[10:11] nt
	s_nop 0
	ds_read_b128 v[248:251], v246 offset:4352
	v_or_b32_e32 v3, 0x18000, v2
	s_waitcnt lgkmcnt(1)
	global_store_dwordx4 v3, v[160:163], s[10:11] nt
	s_nop 0
	ds_read_b128 v[160:163], v246 offset:5440
	v_or_b32_e32 v252, 0x20000, v2
	s_waitcnt lgkmcnt(1)
	global_store_dwordx4 v252, v[248:251], s[10:11] nt
	s_nop 0
	ds_read_b128 v[248:251], v246 offset:6528
	v_or_b32_e32 v3, 0x28000, v2
	s_waitcnt lgkmcnt(1)
	global_store_dwordx4 v3, v[160:163], s[10:11] nt
	s_nop 0
	ds_read_b128 v[160:163], v246 offset:7616
	v_or_b32_e32 v252, 0x30000, v2
	s_waitcnt lgkmcnt(1)
	global_store_dwordx4 v252, v[248:251], s[10:11] nt
	v_or_b32_e32 v3, 0x38000, v2
	s_waitcnt lgkmcnt(0)
	global_store_dwordx4 v3, v[160:163], s[10:11] nt
.Lp2_done:
	v_pk_mul_f32 v[248:249], v[0:1], v[70:71] op_sel_hi:[0,1]
	v_pk_mul_f32 v[250:251], v[0:1], v[76:77] op_sel_hi:[0,1]
	ds_write_b128 v238, v[248:251]
	v_pk_mul_f32 v[248:249], v[0:1], v[78:79] op_sel_hi:[0,1]
	v_pk_mul_f32 v[250:251], v[0:1], v[168:169] op_sel_hi:[0,1]
	ds_write_b128 v238, v[248:251] offset:32
	v_pk_mul_f32 v[248:249], v[0:1], v[126:127] op_sel_hi:[0,1]
	v_pk_mul_f32 v[250:251], v[0:1], v[184:185] op_sel_hi:[0,1]
	ds_write_b128 v238, v[248:251] offset:64
	v_pk_mul_f32 v[248:249], v[0:1], v[186:187] op_sel_hi:[0,1]
	v_pk_mul_f32 v[250:251], v[0:1], v[198:199] op_sel_hi:[0,1]
	ds_write_b128 v238, v[248:251] offset:96
	v_pk_mul_f32 v[248:249], v[0:1], v[196:197] op_sel_hi:[0,1]
	v_pk_mul_f32 v[250:251], v[0:1], v[210:211] op_sel_hi:[0,1]
	ds_write_b128 v238, v[248:251] offset:128
	v_pk_mul_f32 v[248:249], v[0:1], v[212:213] op_sel_hi:[0,1]
	v_pk_mul_f32 v[250:251], v[0:1], v[220:221] op_sel_hi:[0,1]
	ds_write_b128 v238, v[248:251] offset:160
	v_pk_mul_f32 v[248:249], v[0:1], v[218:219] op_sel_hi:[0,1]
	v_pk_mul_f32 v[250:251], v[0:1], v[224:225] op_sel_hi:[0,1]
	ds_write_b128 v238, v[248:251] offset:192
	v_pk_mul_f32 v[248:249], v[0:1], v[226:227] op_sel_hi:[0,1]
	v_pk_mul_f32 v[250:251], v[0:1], v[228:229] op_sel_hi:[0,1]
	ds_write_b128 v238, v[248:251] offset:224
	v_add_u32_e32 v252, 0x300, v253
	v_and_or_b32 v196, v252, s54, v1
	v_add_u32_e32 v252, 0x200, v253
	v_and_or_b32 v198, v252, s54, v1
	s_mov_b32 s72, s55
	s_mov_b32 s73, s56
	s_cmp_lt_u32 s31, 0x200
	s_cbranch_scc0 .Ltail_full
	s_branch .Ltail_end
.Ltail_full:
	v_add_u32_e32 v252, 0x300, v253
	v_and_or_b32 v2, v252, s54, v1
	ds_read_b128 v[248:251], v246
	ds_read_b128 v[160:163], v246 offset:1088
	s_waitcnt lgkmcnt(1)
	global_store_dwordx4 v2, v[248:251], s[10:11] nt
	s_nop 0
	ds_read_b128 v[248:251], v246 offset:2176
	v_or_b32_e32 v3, 0x8000, v2
	s_waitcnt lgkmcnt(1)
	global_store_dwordx4 v3, v[160:163], s[10:11] nt
	s_nop 0
	ds_read_b128 v[160:163], v246 offset:3264
	v_or_b32_e32 v252, 0x10000, v2
	s_waitcnt lgkmcnt(1)
	global_store_dwordx4 v252, v[248:251], s[10:11] nt
	s_nop 0
	ds_read_b128 v[248:251], v246 offset:4352
	v_or_b32_e32 v3, 0x18000, v2
	s_waitcnt lgkmcnt(1)
	global_store_dwordx4 v3, v[160:163], s[10:11] nt
	s_nop 0
	ds_read_b128 v[160:163], v246 offset:5440
	v_or_b32_e32 v252, 0x20000, v2
	s_waitcnt lgkmcnt(1)
	global_store_dwordx4 v252, v[248:251], s[10:11] nt
	s_nop 0
	ds_read_b128 v[248:251], v246 offset:6528
	v_or_b32_e32 v3, 0x28000, v2
	s_waitcnt lgkmcnt(1)
	global_store_dwordx4 v3, v[160:163], s[10:11] nt
	s_nop 0
	ds_read_b128 v[160:163], v246 offset:7616
	v_or_b32_e32 v252, 0x30000, v2
	s_waitcnt lgkmcnt(1)
	global_store_dwordx4 v252, v[248:251], s[10:11] nt
	v_or_b32_e32 v3, 0x38000, v2
	s_waitcnt lgkmcnt(0)
	global_store_dwordx4 v3, v[160:163], s[10:11] nt
.Ltail_end:
	s_mov_b32 s57, s24
	s_add_i32 s12, s12, 4
	s_cmp_eq_u32 s12, 32
	s_cbranch_scc1 .LBB1_22
	s_cmp_lt_u32 s31, 0x200
	s_cbranch_scc0 .LBB1_14
.Lhead_E:
	s_and_b32 s24, s12, 24
	s_or_b32 s56, s24, s27
	s_and_b32 s24, s57, 1
	s_or_b32 s55, s24, s28
	s_add_i32 s24, s55, s29
	s_lshl_b32 s24, s24, 12
	s_lshl_b32 s58, s56, 18
	ds_read_b128 v[64:67], v243
	ds_read_b128 v[68:71], v243 offset:16
	s_waitcnt lgkmcnt(1)
	v_pk_mul_f32 v[76:77], v[64:65], s[22:23] op_sel_hi:[1,0]
	s_waitcnt lgkmcnt(0)
	v_pk_mul_f32 v[64:65], v[68:69], s[22:23] op_sel_hi:[1,0]
	v_pk_mul_f32 v[78:79], v[66:67], s[22:23] op_sel_hi:[1,0]
	v_pk_mul_f32 v[74:75], v[70:71], s[22:23] op_sel_hi:[1,0]
	v_cvt_pk_f16_f32 v204, v64, v65
	ds_read_b128 v[64:67], v243 offset:64
	ds_read_b128 v[68:71], v243 offset:80
	v_cvt_pk_f16_f32 v202, v76, v77
	v_cvt_pk_f16_f32 v205, v74, v75
	v_cvt_pk_f16_f32 v203, v78, v79
	s_waitcnt lgkmcnt(1)
	v_pk_mul_f32 v[76:77], v[64:65], s[22:23] op_sel_hi:[1,0]
	s_waitcnt lgkmcnt(0)
	v_pk_mul_f32 v[64:65], v[68:69], s[22:23] op_sel_hi:[1,0]
	v_pk_mul_f32 v[78:79], v[66:67], s[22:23] op_sel_hi:[1,0]
	v_pk_mul_f32 v[74:75], v[70:71], s[22:23] op_sel_hi:[1,0]
	v_cvt_pk_f16_f32 v208, v64, v65
	ds_read_b128 v[64:67], v243 offset:128
	ds_read_b128 v[68:71], v243 offset:144
	v_cvt_pk_f16_f32 v206, v76, v77
	v_cvt_pk_f16_f32 v209, v74, v75
	v_cvt_pk_f16_f32 v207, v78, v79
	s_waitcnt lgkmcnt(1)
	v_pk_mul_f32 v[76:77], v[64:65], s[22:23] op_sel_hi:[1,0]
	s_waitcnt lgkmcnt(0)
	v_pk_mul_f32 v[64:65], v[68:69], s[22:23] op_sel_hi:[1,0]
	v_pk_mul_f32 v[78:79], v[66:67], s[22:23] op_sel_hi:[1,0]
	v_pk_mul_f32 v[74:75], v[70:71], s[22:23] op_sel_hi:[1,0]
	v_cvt_pk_f16_f32 v212, v64, v65
	ds_read_b128 v[64:67], v243 offset:192
	ds_read_b128 v[68:71], v243 offset:208
	v_cvt_pk_f16_f32 v211, v78, v79
	v_cvt_pk_f16_f32 v210, v76, v77
	v_cvt_pk_f16_f32 v213, v74, v75
	s_waitcnt lgkmcnt(1)
	v_pk_mul_f32 v[78:79], v[66:67], s[22:23] op_sel_hi:[1,0]
	s_waitcnt lgkmcnt(0)
	v_pk_mul_f32 v[66:67], v[70:71], s[22:23] op_sel_hi:[1,0]
	v_pk_mul_f32 v[64:65], v[64:65], s[22:23] op_sel_hi:[1,0]
	v_pk_mul_f32 v[68:69], v[68:69], s[22:23] op_sel_hi:[1,0]
	v_cvt_pk_f16_f32 v214, v64, v65
	v_cvt_pk_f16_f32 v216, v68, v69
	v_cvt_pk_f16_f32 v217, v66, v67
	v_cvt_pk_f16_f32 v215, v78, v79
	s_waitcnt vmcnt(57)
	v_mfma_f32_32x32x16_f16 v[112:127], v[48:51], v[202:205], 0
	s_waitcnt vmcnt(56)
	v_mfma_f32_32x32x16_f16 v[112:127], v[52:55], v[206:209], v[112:127]
	s_waitcnt vmcnt(55)
	v_mfma_f32_32x32x16_f16 v[112:127], v[56:59], v[210:213], v[112:127]
	s_waitcnt vmcnt(54)
	v_mfma_f32_32x32x16_f16 v[112:127], v[60:63], v[214:217], v[112:127]
	s_waitcnt vmcnt(34)
	v_mfma_f32_32x32x16_f16 v[48:63], v[32:35], v[202:205], 0
	s_waitcnt vmcnt(33)
	v_mfma_f32_32x32x16_f16 v[48:63], v[36:39], v[206:209], v[48:63]
	v_mfma_f32_32x32x16_f16 v[48:63], v[40:43], v[210:213], v[48:63]
	v_mfma_f32_32x32x16_f16 v[48:63], v[44:47], v[214:217], v[48:63]
	s_waitcnt vmcnt(32)
	v_mfma_f32_32x32x16_f16 v[32:47], v[16:19], v[202:205], 0
	s_waitcnt vmcnt(31)
	v_mfma_f32_32x32x16_f16 v[32:47], v[20:23], v[206:209], v[32:47]
	s_waitcnt vmcnt(30)
	v_mfma_f32_32x32x16_f16 v[32:47], v[24:27], v[210:213], v[32:47]
	s_waitcnt vmcnt(29)
	v_mfma_f32_32x32x16_f16 v[32:47], v[28:31], v[214:217], v[32:47]
	s_waitcnt vmcnt(28)
	v_mfma_f32_32x32x16_f16 v[16:31], v[4:7], v[202:205], 0
	s_waitcnt vmcnt(27)
	v_mfma_f32_32x32x16_f16 v[16:31], v[8:11], v[206:209], v[16:31]
	s_waitcnt vmcnt(26)
	v_mfma_f32_32x32x16_f16 v[16:31], v[12:15], v[210:213], v[16:31]
	v_mfma_f32_32x32x16_f16 v[16:31], v[148:151], v[214:217], v[16:31]
	v_mfma_f32_32x32x16_f16 v[0:15], v[132:135], v[202:205], 0
	v_mfma_f32_32x32x16_f16 v[0:15], v[136:139], v[206:209], v[0:15]
	v_mfma_f32_32x32x16_f16 v[0:15], v[140:143], v[210:213], v[0:15]
	v_mfma_f32_32x32x16_f16 v[0:15], v[144:147], v[214:217], v[0:15]
	s_waitcnt vmcnt(9)
	v_mfma_f32_32x32x16_f16 v[64:79], v[80:83], v[202:205], 0
	s_waitcnt vmcnt(8)
	v_mfma_f32_32x32x16_f16 v[64:79], v[84:87], v[206:209], v[64:79]
	s_waitcnt vmcnt(7)
	v_mfma_f32_32x32x16_f16 v[64:79], v[88:91], v[210:213], v[64:79]
	s_waitcnt vmcnt(6)
	v_mfma_f32_32x32x16_f16 v[64:79], v[92:95], v[214:217], v[64:79]
	s_waitcnt vmcnt(5)
	v_mfma_f32_32x32x16_f16 v[80:95], v[96:99], v[202:205], 0
	s_waitcnt vmcnt(4)
	v_mfma_f32_32x32x16_f16 v[80:95], v[100:103], v[206:209], v[80:95]
	s_waitcnt vmcnt(3)
	v_mfma_f32_32x32x16_f16 v[80:95], v[108:111], v[210:213], v[80:95]
	s_waitcnt vmcnt(2)
	v_mfma_f32_32x32x16_f16 v[80:95], v[192:195], v[214:217], v[80:95]
	v_mfma_f32_32x32x16_f16 v[96:111], v[152:155], v[202:205], 0
	v_mfma_f32_32x32x16_f16 v[96:111], v[156:159], v[206:209], v[96:111]
	s_waitcnt vmcnt(1)
	v_mfma_f32_32x32x16_f16 v[96:111], v[174:177], v[210:213], v[96:111]
	s_waitcnt vmcnt(0)
	v_mfma_f32_32x32x16_f16 v[96:111], v[178:181], v[214:217], v[96:111]
	s_branch .Lafter_qk
.LBB1_14:
	s_and_b32 s24, s12, 24
	s_or_b32 s56, s24, s27
	s_and_b32 s24, s57, 1
	s_or_b32 s55, s24, s28
	s_add_i32 s24, s55, s29
	s_lshl_b32 s24, s24, 12
	s_lshl_b32 s58, s56, 18
	ds_read_b128 v[64:67], v243
	ds_read_b128 v[68:71], v243 offset:16
	s_waitcnt lgkmcnt(1)
	v_pk_mul_f32 v[76:77], v[64:65], s[22:23] op_sel_hi:[1,0]
	s_waitcnt lgkmcnt(0)
	v_pk_mul_f32 v[64:65], v[68:69], s[22:23] op_sel_hi:[1,0]
	v_pk_mul_f32 v[78:79], v[66:67], s[22:23] op_sel_hi:[1,0]
	v_pk_mul_f32 v[74:75], v[70:71], s[22:23] op_sel_hi:[1,0]
	v_cvt_pk_f16_f32 v204, v64, v65
	ds_read_b128 v[64:67], v243 offset:64
	ds_read_b128 v[68:71], v243 offset:80
	v_cvt_pk_f16_f32 v202, v76, v77
	v_cvt_pk_f16_f32 v205, v74, v75
	v_cvt_pk_f16_f32 v203, v78, v79
	s_waitcnt lgkmcnt(1)
	v_pk_mul_f32 v[76:77], v[64:65], s[22:23] op_sel_hi:[1,0]
	s_waitcnt lgkmcnt(0)
	v_pk_mul_f32 v[64:65], v[68:69], s[22:23] op_sel_hi:[1,0]
	v_pk_mul_f32 v[78:79], v[66:67], s[22:23] op_sel_hi:[1,0]
	v_pk_mul_f32 v[74:75], v[70:71], s[22:23] op_sel_hi:[1,0]
	v_cvt_pk_f16_f32 v208, v64, v65
	ds_read_b128 v[64:67], v243 offset:128
	ds_read_b128 v[68:71], v243 offset:144
	v_cvt_pk_f16_f32 v206, v76, v77
	v_cvt_pk_f16_f32 v209, v74, v75
	v_cvt_pk_f16_f32 v207, v78, v79
	s_waitcnt lgkmcnt(1)
	v_pk_mul_f32 v[76:77], v[64:65], s[22:23] op_sel_hi:[1,0]
	s_waitcnt lgkmcnt(0)
	v_pk_mul_f32 v[64:65], v[68:69], s[22:23] op_sel_hi:[1,0]
	v_pk_mul_f32 v[78:79], v[66:67], s[22:23] op_sel_hi:[1,0]
	v_pk_mul_f32 v[74:75], v[70:71], s[22:23] op_sel_hi:[1,0]
	v_cvt_pk_f16_f32 v212, v64, v65
	ds_read_b128 v[64:67], v243 offset:192
	ds_read_b128 v[68:71], v243 offset:208
	v_cvt_pk_f16_f32 v211, v78, v79
	v_cvt_pk_f16_f32 v210, v76, v77
	v_cvt_pk_f16_f32 v213, v74, v75
	s_waitcnt lgkmcnt(1)
	v_pk_mul_f32 v[78:79], v[66:67], s[22:23] op_sel_hi:[1,0]
	s_waitcnt lgkmcnt(0)
	v_pk_mul_f32 v[66:67], v[70:71], s[22:23] op_sel_hi:[1,0]
	v_pk_mul_f32 v[64:65], v[64:65], s[22:23] op_sel_hi:[1,0]
	v_pk_mul_f32 v[68:69], v[68:69], s[22:23] op_sel_hi:[1,0]
	v_cvt_pk_f16_f32 v214, v64, v65
	v_cvt_pk_f16_f32 v216, v68, v69
	v_cvt_pk_f16_f32 v217, v66, v67
	v_cvt_pk_f16_f32 v215, v78, v79
	s_waitcnt vmcnt(57)
	v_mfma_f32_32x32x16_f16 v[112:127], v[48:51], v[202:205], 0
	s_waitcnt vmcnt(56)
	v_mfma_f32_32x32x16_f16 v[112:127], v[52:55], v[206:209], v[112:127]
	s_waitcnt vmcnt(55)
	v_mfma_f32_32x32x16_f16 v[112:127], v[56:59], v[210:213], v[112:127]
	s_waitcnt vmcnt(54)
	v_mfma_f32_32x32x16_f16 v[112:127], v[60:63], v[214:217], v[112:127]
	s_waitcnt vmcnt(50)
	v_mfma_f32_32x32x16_f16 v[48:63], v[32:35], v[202:205], 0
	s_waitcnt vmcnt(49)
	v_mfma_f32_32x32x16_f16 v[48:63], v[36:39], v[206:209], v[48:63]
	v_mfma_f32_32x32x16_f16 v[48:63], v[40:43], v[210:213], v[48:63]
	v_mfma_f32_32x32x16_f16 v[48:63], v[44:47], v[214:217], v[48:63]
	s_waitcnt vmcnt(48)
	v_mfma_f32_32x32x16_f16 v[32:47], v[16:19], v[202:205], 0
	s_waitcnt vmcnt(47)
	v_mfma_f32_32x32x16_f16 v[32:47], v[20:23], v[206:209], v[32:47]
	s_waitcnt vmcnt(46)
	v_mfma_f32_32x32x16_f16 v[32:47], v[24:27], v[210:213], v[32:47]
	s_waitcnt vmcnt(45)
	v_mfma_f32_32x32x16_f16 v[32:47], v[28:31], v[214:217], v[32:47]
	s_waitcnt vmcnt(44)
	v_mfma_f32_32x32x16_f16 v[16:31], v[4:7], v[202:205], 0
	s_waitcnt vmcnt(43)
	v_mfma_f32_32x32x16_f16 v[16:31], v[8:11], v[206:209], v[16:31]
	s_waitcnt vmcnt(42)
	v_mfma_f32_32x32x16_f16 v[16:31], v[12:15], v[210:213], v[16:31]
	v_mfma_f32_32x32x16_f16 v[16:31], v[148:151], v[214:217], v[16:31]
	v_mfma_f32_32x32x16_f16 v[0:15], v[132:135], v[202:205], 0
	v_mfma_f32_32x32x16_f16 v[0:15], v[136:139], v[206:209], v[0:15]
	v_mfma_f32_32x32x16_f16 v[0:15], v[140:143], v[210:213], v[0:15]
	v_mfma_f32_32x32x16_f16 v[0:15], v[144:147], v[214:217], v[0:15]
	s_waitcnt vmcnt(25)
	v_mfma_f32_32x32x16_f16 v[64:79], v[80:83], v[202:205], 0
	s_waitcnt vmcnt(24)
	v_mfma_f32_32x32x16_f16 v[64:79], v[84:87], v[206:209], v[64:79]
	s_waitcnt vmcnt(23)
	v_mfma_f32_32x32x16_f16 v[64:79], v[88:91], v[210:213], v[64:79]
	s_waitcnt vmcnt(22)
	v_mfma_f32_32x32x16_f16 v[64:79], v[92:95], v[214:217], v[64:79]
	s_waitcnt vmcnt(21)
	v_mfma_f32_32x32x16_f16 v[80:95], v[96:99], v[202:205], 0
	s_waitcnt vmcnt(20)
	v_mfma_f32_32x32x16_f16 v[80:95], v[100:103], v[206:209], v[80:95]
	s_waitcnt vmcnt(19)
	v_mfma_f32_32x32x16_f16 v[80:95], v[108:111], v[210:213], v[80:95]
	s_waitcnt vmcnt(18)
	v_mfma_f32_32x32x16_f16 v[80:95], v[192:195], v[214:217], v[80:95]
	v_mfma_f32_32x32x16_f16 v[96:111], v[152:155], v[202:205], 0
	v_mfma_f32_32x32x16_f16 v[96:111], v[156:159], v[206:209], v[96:111]
	s_waitcnt vmcnt(17)
	v_mfma_f32_32x32x16_f16 v[96:111], v[174:177], v[210:213], v[96:111]
	s_waitcnt vmcnt(16)
	v_mfma_f32_32x32x16_f16 v[96:111], v[178:181], v[214:217], v[96:111]
.Lafter_qk:
	s_and_b32 s25, s24, 0x3f000
	s_addk_i32 s24, 0x1000
	s_or_b32 s25, s58, s25
	s_and_b32 s24, s24, 0x3f000
	v_or_b32_e32 v132, s25, v231
	s_or_b32 s24, s58, s24
	global_load_dwordx4 v[156:159], v132, s[16:17]
	global_load_dwordx4 v[160:163], v132, s[16:17] offset:1024
	global_load_dwordx4 v[152:155], v132, s[16:17] offset:2048
	global_load_dwordx4 v[148:151], v132, s[16:17] offset:3072
	v_or_b32_e32 v132, s24, v231
	global_load_dwordx4 v[144:147], v132, s[16:17]
	global_load_dwordx4 v[140:143], v132, s[16:17] offset:1024
	global_load_dwordx4 v[136:139], v132, s[16:17] offset:2048
	s_nop 0
	global_load_dwordx4 v[132:135], v132, s[16:17] offset:3072
	v_max_f32_e32 v166, v113, v113
	v_max_f32_e32 v167, v112, v112
	v_max_f32_e32 v166, v167, v166
	v_max3_f32 v166, v166, v114, v115
	v_max3_f32 v166, v166, v116, v117
	v_max3_f32 v166, v166, v118, v119
	v_max3_f32 v166, v166, v120, v121
	v_max3_f32 v166, v166, v122, v123
	v_max3_f32 v166, v166, v124, v125
	v_max3_f32 v166, v166, v126, v127
	v_max3_f32 v166, v166, v96, v97
	v_max3_f32 v166, v166, v98, v99
	v_max3_f32 v166, v166, v100, v101
	v_max3_f32 v166, v166, v102, v103
	v_max3_f32 v166, v166, v104, v105
	v_max3_f32 v166, v166, v106, v107
	v_max3_f32 v166, v166, v108, v109
	v_max3_f32 v166, v166, v110, v111
	v_max3_f32 v166, v166, v80, v81
	v_max3_f32 v166, v166, v82, v83
	v_max3_f32 v166, v166, v84, v85
	v_max3_f32 v166, v166, v86, v87
	v_max3_f32 v166, v166, v88, v89
	v_max3_f32 v166, v166, v90, v91
	v_max3_f32 v166, v166, v92, v93
	v_max3_f32 v166, v166, v94, v95
	v_max3_f32 v166, v166, v64, v65
	v_max3_f32 v166, v166, v66, v67
	v_max3_f32 v166, v166, v68, v69
	v_max3_f32 v166, v166, v70, v71
	v_max3_f32 v166, v166, v72, v73
	v_max3_f32 v166, v166, v74, v75
	v_max3_f32 v166, v166, v76, v77
	v_max3_f32 v166, v166, v78, v79
	v_max3_f32 v166, v166, v48, v49
	v_max3_f32 v166, v166, v50, v51
	v_max3_f32 v166, v166, v52, v53
	v_max3_f32 v166, v166, v54, v55
	v_max3_f32 v166, v166, v56, v57
	v_max3_f32 v166, v166, v58, v59
	v_max3_f32 v166, v166, v60, v61
	v_max3_f32 v166, v166, v62, v63
	v_max3_f32 v166, v166, v32, v33
	v_max3_f32 v166, v166, v34, v35
	v_max3_f32 v166, v166, v36, v37
	v_max3_f32 v166, v166, v38, v39
	v_max3_f32 v166, v166, v40, v41
	v_max3_f32 v166, v166, v42, v43
	v_max3_f32 v166, v166, v44, v45
	v_max3_f32 v166, v166, v46, v47
	v_max3_f32 v166, v166, v16, v17
	v_max3_f32 v166, v166, v18, v19
	v_max3_f32 v166, v166, v20, v21
	v_max3_f32 v166, v166, v22, v23
	v_max3_f32 v166, v166, v24, v25
	v_max3_f32 v166, v166, v26, v27
	v_max3_f32 v166, v166, v28, v29
	v_max3_f32 v166, v166, v30, v31
	v_max3_f32 v166, v166, v0, v1
	v_max3_f32 v166, v166, v2, v3
	v_max3_f32 v166, v166, v4, v5
	v_max3_f32 v166, v166, v6, v7
	v_max3_f32 v166, v166, v8, v9
	v_max3_f32 v166, v166, v10, v11
	v_max3_f32 v166, v166, v12, v13
	v_max3_f32 v166, v166, v14, v15
	ds_bpermute_b32 v167, v234, v166
	s_waitcnt lgkmcnt(0)
	v_max_f32_e32 v167, v167, v167
	v_max_f32_e32 v247, v166, v167
	s_and_saveexec_b64 s[24:25], s[0:1]
	v_add_u32_e32 v166, s31, v235
	ds_write_b32 v166, v247
	s_or_b64 exec, exec, s[24:25]
	v_sub_f32_e32 v112, v112, v247
	v_exp_f32_e32 v208, v112
	v_sub_f32_e32 v112, v113, v247
	v_exp_f32_e32 v209, v112
	v_sub_f32_e32 v112, v114, v247
	v_exp_f32_e32 v204, v112
	v_sub_f32_e32 v112, v115, v247
	v_exp_f32_e32 v205, v112
	v_sub_f32_e32 v113, v116, v247
	v_add_f32_e32 v112, 0, v208
	v_exp_f32_e32 v182, v113
	v_sub_f32_e32 v113, v117, v247
	v_add_f32_e32 v112, v112, v209
	v_exp_f32_e32 v183, v113
	v_sub_f32_e32 v113, v118, v247
	v_add_f32_e32 v112, v112, v204
	v_exp_f32_e32 v178, v113
	v_sub_f32_e32 v113, v119, v247
	v_add_f32_e32 v112, v112, v205
	v_exp_f32_e32 v179, v113
	v_sub_f32_e32 v113, v120, v247
	v_add_f32_e32 v112, v112, v182
	v_exp_f32_e32 v166, v113
	v_sub_f32_e32 v113, v121, v247
	v_add_f32_e32 v112, v112, v183
	v_exp_f32_e32 v167, v113
	v_sub_f32_e32 v113, v122, v247
	v_add_f32_e32 v112, v112, v178
	v_exp_f32_e32 v118, v113
	v_sub_f32_e32 v113, v123, v247
	v_add_f32_e32 v112, v112, v179
	v_exp_f32_e32 v119, v113
	v_sub_f32_e32 v113, v124, v247
	v_add_f32_e32 v112, v112, v166
	v_exp_f32_e32 v116, v113
	v_sub_f32_e32 v113, v125, v247
	v_add_f32_e32 v112, v112, v167
	v_exp_f32_e32 v117, v113
	v_sub_f32_e32 v113, v126, v247
	v_add_f32_e32 v112, v112, v118
	v_exp_f32_e32 v114, v113
	v_sub_f32_e32 v113, v127, v247
	v_add_f32_e32 v112, v112, v119
	v_exp_f32_e32 v115, v113
	v_add_f32_e32 v112, v112, v116
	v_add_f32_e32 v112, v112, v117
	v_add_f32_e32 v112, v112, v114
	v_sub_f32_e32 v96, v96, v247
	v_add_f32_e32 v120, v112, v115
	v_exp_f32_e32 v112, v96
	v_sub_f32_e32 v96, v97, v247
	v_exp_f32_e32 v113, v96
	v_sub_f32_e32 v96, v98, v247
	v_exp_f32_e32 v98, v96
	v_sub_f32_e32 v96, v99, v247
	v_exp_f32_e32 v99, v96
	v_sub_f32_e32 v97, v100, v247
	v_add_f32_e32 v96, v120, v112
	v_exp_f32_e32 v100, v97
	v_sub_f32_e32 v97, v101, v247
	v_add_f32_e32 v96, v96, v113
	v_exp_f32_e32 v101, v97
	v_sub_f32_e32 v97, v102, v247
	v_add_f32_e32 v96, v96, v98
	v_exp_f32_e32 v120, v97
	v_sub_f32_e32 v97, v103, v247
	v_add_f32_e32 v96, v96, v99
	v_exp_f32_e32 v121, v97
	v_sub_f32_e32 v97, v104, v247
	v_add_f32_e32 v96, v96, v100
	v_exp_f32_e32 v102, v97
	v_sub_f32_e32 v97, v105, v247
	v_add_f32_e32 v96, v96, v101
	v_exp_f32_e32 v103, v97
	v_sub_f32_e32 v97, v106, v247
	v_add_f32_e32 v96, v96, v120
	v_exp_f32_e32 v122, v97
	v_sub_f32_e32 v97, v107, v247
	v_add_f32_e32 v96, v96, v121
	v_exp_f32_e32 v123, v97
	v_sub_f32_e32 v97, v108, v247
	v_add_f32_e32 v96, v96, v102
	v_exp_f32_e32 v124, v97
	v_sub_f32_e32 v97, v109, v247
	v_add_f32_e32 v96, v96, v103
	v_exp_f32_e32 v125, v97
	v_sub_f32_e32 v97, v110, v247
	v_add_f32_e32 v96, v96, v122
	v_exp_f32_e32 v180, v97
	v_sub_f32_e32 v97, v111, v247
	v_add_f32_e32 v96, v96, v123
	v_exp_f32_e32 v181, v97
	v_sub_f32_e32 v80, v80, v247
	v_add_f32_e32 v96, v96, v124
	v_exp_f32_e32 v80, v80
	v_sub_f32_e32 v81, v81, v247
	v_add_f32_e32 v96, v96, v125
	v_exp_f32_e32 v81, v81
	v_sub_f32_e32 v82, v82, v247
	v_add_f32_e32 v96, v96, v180
	v_exp_f32_e32 v82, v82
	v_sub_f32_e32 v83, v83, v247
	v_add_f32_e32 v96, v96, v181
	v_exp_f32_e32 v83, v83
	v_add_f32_e32 v96, v96, v80
	v_sub_f32_e32 v84, v84, v247
	v_add_f32_e32 v96, v96, v81
	v_exp_f32_e32 v84, v84
	v_sub_f32_e32 v85, v85, v247
	v_add_f32_e32 v96, v96, v82
	v_exp_f32_e32 v85, v85
	v_sub_f32_e32 v86, v86, v247
	v_add_f32_e32 v104, v96, v83
	v_exp_f32_e32 v96, v86
	v_sub_f32_e32 v86, v87, v247
	v_exp_f32_e32 v97, v86
	v_add_f32_e32 v86, v104, v84
	v_add_f32_e32 v86, v86, v85
	v_add_f32_e32 v86, v86, v96
	v_add_f32_e32 v104, v86, v97
	v_sub_f32_e32 v86, v88, v247
	v_exp_f32_e32 v86, v86
	v_sub_f32_e32 v87, v89, v247
	v_exp_f32_e32 v87, v87
	v_sub_f32_e32 v88, v90, v247
	v_exp_f32_e32 v88, v88
	v_sub_f32_e32 v89, v91, v247
	v_exp_f32_e32 v89, v89
	v_add_f32_e32 v90, v104, v86
	v_add_f32_e32 v90, v90, v87
	v_add_f32_e32 v90, v90, v88
	v_add_f32_e32 v104, v90, v89
	v_sub_f32_e32 v90, v92, v247
	v_exp_f32_e32 v90, v90
	v_sub_f32_e32 v91, v93, v247
	v_exp_f32_e32 v91, v91
	v_sub_f32_e32 v92, v94, v247
	v_exp_f32_e32 v94, v92
	v_sub_f32_e32 v92, v95, v247
	v_exp_f32_e32 v95, v92
	v_add_f32_e32 v92, v104, v90
	v_add_f32_e32 v92, v92, v91
	v_add_f32_e32 v92, v92, v94
	v_sub_f32_e32 v64, v64, v247
	v_add_f32_e32 v104, v92, v95
	v_exp_f32_e32 v92, v64
	v_sub_f32_e32 v64, v65, v247
	v_exp_f32_e32 v93, v64
	v_sub_f32_e32 v64, v66, v247
	v_exp_f32_e32 v108, v64
	v_sub_f32_e32 v64, v67, v247
	v_exp_f32_e32 v109, v64
	v_sub_f32_e32 v65, v68, v247
	v_add_f32_e32 v64, v104, v92
	v_exp_f32_e32 v110, v65
	v_sub_f32_e32 v65, v69, v247
	v_add_f32_e32 v64, v64, v93
	v_exp_f32_e32 v111, v65
	v_sub_f32_e32 v65, v70, v247
	v_add_f32_e32 v64, v64, v108
	v_exp_f32_e32 v176, v65
	v_sub_f32_e32 v65, v71, v247
	v_add_f32_e32 v64, v64, v109
	v_exp_f32_e32 v177, v65
	v_sub_f32_e32 v65, v72, v247
	v_add_f32_e32 v64, v64, v110
	v_exp_f32_e32 v174, v65
	v_sub_f32_e32 v65, v73, v247
	v_add_f32_e32 v64, v64, v111
	v_exp_f32_e32 v175, v65
	v_sub_f32_e32 v65, v74, v247
	v_add_f32_e32 v64, v64, v176
	v_exp_f32_e32 v192, v65
	v_sub_f32_e32 v65, v75, v247
	v_add_f32_e32 v64, v64, v177
	v_exp_f32_e32 v193, v65
	v_sub_f32_e32 v65, v76, v247
	v_add_f32_e32 v64, v64, v174
	v_exp_f32_e32 v194, v65
	v_sub_f32_e32 v65, v77, v247
	v_add_f32_e32 v64, v64, v175
	v_exp_f32_e32 v195, v65
	v_sub_f32_e32 v65, v78, v247
	v_add_f32_e32 v64, v64, v192
	v_exp_f32_e32 v206, v65
	v_sub_f32_e32 v65, v79, v247
	v_add_f32_e32 v64, v64, v193
	v_exp_f32_e32 v207, v65
	v_add_f32_e32 v64, v64, v194
	v_add_f32_e32 v64, v64, v195
	v_add_f32_e32 v64, v64, v206
	v_sub_f32_e32 v48, v48, v247
	v_add_f32_e32 v68, v64, v207
	v_exp_f32_e32 v64, v48
	v_sub_f32_e32 v48, v49, v247
	v_exp_f32_e32 v65, v48
	v_sub_f32_e32 v48, v50, v247
	v_exp_f32_e32 v66, v48
	v_sub_f32_e32 v48, v51, v247
	v_exp_f32_e32 v67, v48
	v_sub_f32_e32 v49, v52, v247
	v_add_f32_e32 v48, v68, v64
	v_exp_f32_e32 v68, v49
	v_sub_f32_e32 v49, v53, v247
	v_add_f32_e32 v48, v48, v65
	v_exp_f32_e32 v69, v49
	v_sub_f32_e32 v49, v54, v247
	v_add_f32_e32 v48, v48, v66
	v_exp_f32_e32 v74, v49
	v_sub_f32_e32 v49, v55, v247
	v_add_f32_e32 v48, v48, v67
	v_exp_f32_e32 v75, v49
	v_sub_f32_e32 v49, v56, v247
	v_add_f32_e32 v48, v48, v68
	v_exp_f32_e32 v72, v49
	v_sub_f32_e32 v49, v57, v247
	v_add_f32_e32 v48, v48, v69
	v_exp_f32_e32 v73, v49
	v_sub_f32_e32 v49, v58, v247
	v_add_f32_e32 v48, v48, v74
	v_exp_f32_e32 v104, v49
	v_sub_f32_e32 v49, v59, v247
	v_add_f32_e32 v48, v48, v75
	v_exp_f32_e32 v105, v49
	v_sub_f32_e32 v49, v60, v247
	v_add_f32_e32 v48, v48, v72
	v_exp_f32_e32 v106, v49
	v_sub_f32_e32 v49, v61, v247
	v_add_f32_e32 v48, v48, v73
	v_exp_f32_e32 v107, v49
	v_sub_f32_e32 v49, v62, v247
	v_add_f32_e32 v48, v48, v104
	v_exp_f32_e32 v172, v49
	v_sub_f32_e32 v49, v63, v247
	v_add_f32_e32 v48, v48, v105
	v_exp_f32_e32 v173, v49
	v_sub_f32_e32 v32, v32, v247
	v_add_f32_e32 v48, v48, v106
	v_exp_f32_e32 v170, v32
	v_sub_f32_e32 v32, v33, v247
	v_add_f32_e32 v48, v48, v107
	v_exp_f32_e32 v171, v32
	v_sub_f32_e32 v32, v34, v247
	v_add_f32_e32 v48, v48, v172
	v_exp_f32_e32 v188, v32
	v_sub_f32_e32 v32, v35, v247
	v_add_f32_e32 v48, v48, v173
	v_exp_f32_e32 v189, v32
	v_sub_f32_e32 v33, v36, v247
	v_add_f32_e32 v32, v48, v170
	v_exp_f32_e32 v190, v33
	v_sub_f32_e32 v33, v37, v247
	v_add_f32_e32 v32, v32, v171
	v_exp_f32_e32 v191, v33
	v_sub_f32_e32 v33, v38, v247
	v_add_f32_e32 v32, v32, v188
	v_exp_f32_e32 v202, v33
	v_sub_f32_e32 v33, v39, v247
	v_add_f32_e32 v32, v32, v189
	v_exp_f32_e32 v203, v33
	v_sub_f32_e32 v33, v40, v247
	v_add_f32_e32 v32, v32, v190
	v_exp_f32_e32 v200, v33
	v_sub_f32_e32 v33, v41, v247
	v_add_f32_e32 v32, v32, v191
	v_exp_f32_e32 v201, v33
	v_sub_f32_e32 v33, v42, v247
	v_add_f32_e32 v32, v32, v202
	v_exp_f32_e32 v214, v33
	v_sub_f32_e32 v33, v43, v247
	v_add_f32_e32 v32, v32, v203
	v_exp_f32_e32 v215, v33
	v_sub_f32_e32 v33, v44, v247
	v_add_f32_e32 v32, v32, v200
	v_exp_f32_e32 v216, v33
	v_sub_f32_e32 v33, v45, v247
	v_add_f32_e32 v32, v32, v201
	v_exp_f32_e32 v217, v33
	v_sub_f32_e32 v33, v46, v247
	v_add_f32_e32 v32, v32, v214
	v_exp_f32_e32 v222, v33
	v_sub_f32_e32 v33, v47, v247
	v_add_f32_e32 v32, v32, v215
	v_exp_f32_e32 v223, v33
	v_sub_f32_e32 v16, v16, v247
	v_add_f32_e32 v32, v32, v216
	v_exp_f32_e32 v70, v16
	v_sub_f32_e32 v16, v17, v247
	v_add_f32_e32 v32, v32, v217
	v_exp_f32_e32 v71, v16
	v_sub_f32_e32 v16, v18, v247
	v_add_f32_e32 v32, v32, v222
	v_exp_f32_e32 v76, v16
	v_sub_f32_e32 v16, v19, v247
	v_add_f32_e32 v32, v32, v223
	v_exp_f32_e32 v77, v16
	v_sub_f32_e32 v17, v20, v247
	v_add_f32_e32 v16, v32, v70
	v_exp_f32_e32 v78, v17
	v_sub_f32_e32 v17, v21, v247
	v_add_f32_e32 v16, v16, v71
	v_exp_f32_e32 v79, v17
	v_sub_f32_e32 v17, v22, v247
	v_add_f32_e32 v16, v16, v76
	v_exp_f32_e32 v168, v17
	v_sub_f32_e32 v17, v23, v247
	v_add_f32_e32 v16, v16, v77
	v_exp_f32_e32 v169, v17
	v_sub_f32_e32 v17, v24, v247
	v_add_f32_e32 v16, v16, v78
	v_exp_f32_e32 v126, v17
	v_sub_f32_e32 v17, v25, v247
	v_add_f32_e32 v16, v16, v79
	v_exp_f32_e32 v127, v17
	v_sub_f32_e32 v17, v26, v247
	v_add_f32_e32 v16, v16, v168
	v_exp_f32_e32 v184, v17
	v_sub_f32_e32 v17, v27, v247
	v_add_f32_e32 v16, v16, v169
	v_exp_f32_e32 v185, v17
	v_sub_f32_e32 v17, v28, v247
	v_add_f32_e32 v16, v16, v126
	v_exp_f32_e32 v186, v17
	v_sub_f32_e32 v17, v29, v247
	v_add_f32_e32 v16, v16, v127
	v_exp_f32_e32 v187, v17
	v_sub_f32_e32 v17, v30, v247
	v_add_f32_e32 v16, v16, v184
	v_exp_f32_e32 v198, v17
	v_sub_f32_e32 v17, v31, v247
	v_add_f32_e32 v16, v16, v185
	v_exp_f32_e32 v199, v17
	v_sub_f32_e32 v0, v0, v247
	v_add_f32_e32 v16, v16, v186
	v_exp_f32_e32 v196, v0
	v_sub_f32_e32 v0, v1, v247
	v_add_f32_e32 v16, v16, v187
	v_exp_f32_e32 v197, v0
	v_sub_f32_e32 v0, v2, v247
	v_add_f32_e32 v16, v16, v198
	v_exp_f32_e32 v210, v0
	v_sub_f32_e32 v0, v3, v247
	v_add_f32_e32 v16, v16, v199
	v_exp_f32_e32 v211, v0
	v_sub_f32_e32 v1, v4, v247
	v_add_f32_e32 v0, v16, v196
	v_exp_f32_e32 v212, v1
	v_sub_f32_e32 v1, v5, v247
	v_add_f32_e32 v0, v0, v197
	v_exp_f32_e32 v213, v1
	v_sub_f32_e32 v1, v6, v247
	v_add_f32_e32 v0, v0, v210
	v_exp_f32_e32 v220, v1
	v_sub_f32_e32 v1, v7, v247
	v_add_f32_e32 v0, v0, v211
	v_exp_f32_e32 v221, v1
	v_sub_f32_e32 v1, v8, v247
	v_add_f32_e32 v0, v0, v212
	v_exp_f32_e32 v218, v1
	v_sub_f32_e32 v1, v9, v247
	v_add_f32_e32 v0, v0, v213
	v_exp_f32_e32 v219, v1
	v_sub_f32_e32 v1, v10, v247
	v_add_f32_e32 v0, v0, v220
	v_exp_f32_e32 v224, v1
	v_sub_f32_e32 v1, v11, v247
	v_add_f32_e32 v0, v0, v221
	v_exp_f32_e32 v225, v1
	v_sub_f32_e32 v1, v12, v247
	v_add_f32_e32 v0, v0, v218
	v_exp_f32_e32 v226, v1
	v_sub_f32_e32 v1, v13, v247
	v_add_f32_e32 v0, v0, v219
	v_exp_f32_e32 v227, v1
	v_sub_f32_e32 v1, v14, v247
	v_add_f32_e32 v0, v0, v224
	v_exp_f32_e32 v228, v1
	v_sub_f32_e32 v1, v15, v247
	v_add_f32_e32 v0, v0, v225
	v_exp_f32_e32 v229, v1
	v_add_f32_e32 v0, v0, v226
	v_add_f32_e32 v0, v0, v227
	v_add_f32_e32 v0, v0, v228
	v_add_f32_e32 v0, v0, v229
	ds_bpermute_b32 v1, v234, v0
	s_and_saveexec_b64 s[24:25], s[0:1]
	s_cbranch_execz .LBB1_18
	s_waitcnt lgkmcnt(0)
	v_add_f32_e32 v0, v0, v1
	v_add_u32_e32 v1, s31, v236
	ds_write_b32 v1, v0

.LBB1_22:
	s_cmp_lt_u32 s31, 0x200
	s_cbranch_scc0 .Lx_p3
	v_subrev_u32_e32 v160, 0x13200, v246
	ds_read_b128 v[184:187], v160
	ds_read_b128 v[188:191], v160 offset:1088
	s_waitcnt lgkmcnt(1)
	global_store_dwordx4 v198, v[184:187], s[10:11] nt
	s_nop 0
	ds_read_b128 v[184:187], v160 offset:2176
	v_or_b32_e32 v199, 0x8000, v198
	s_waitcnt lgkmcnt(1)
	global_store_dwordx4 v199, v[188:191], s[10:11] nt
	s_nop 0
	ds_read_b128 v[188:191], v160 offset:3264
	v_or_b32_e32 v199, 0x10000, v198
	s_waitcnt lgkmcnt(1)
	global_store_dwordx4 v199, v[184:187], s[10:11] nt
	s_nop 0
	ds_read_b128 v[184:187], v160 offset:4352
	v_or_b32_e32 v199, 0x18000, v198
	s_waitcnt lgkmcnt(1)
	global_store_dwordx4 v199, v[188:191], s[10:11] nt
	s_nop 0
	ds_read_b128 v[188:191], v160 offset:5440
	v_or_b32_e32 v199, 0x20000, v198
	s_waitcnt lgkmcnt(1)
	global_store_dwordx4 v199, v[184:187], s[10:11] nt
	s_nop 0
	ds_read_b128 v[184:187], v160 offset:6528
	v_or_b32_e32 v199, 0x28000, v198
	s_waitcnt lgkmcnt(1)
	global_store_dwordx4 v199, v[188:191], s[10:11] nt
	s_nop 0
	ds_read_b128 v[188:191], v160 offset:7616
	v_or_b32_e32 v199, 0x30000, v198
	s_waitcnt lgkmcnt(1)
	global_store_dwordx4 v199, v[184:187], s[10:11] nt
	v_or_b32_e32 v199, 0x38000, v198
	s_waitcnt lgkmcnt(0)
	global_store_dwordx4 v199, v[188:191], s[10:11] nt
.Lx_p3:
	s_cmp_lt_u32 s31, 0x200
	s_cbranch_scc0 .Lall_done
	ds_read_b128 v[184:187], v246
	ds_read_b128 v[188:191], v246 offset:1088
	s_waitcnt lgkmcnt(1)
	global_store_dwordx4 v196, v[184:187], s[10:11] nt
	s_nop 0
	ds_read_b128 v[184:187], v246 offset:2176
	v_or_b32_e32 v197, 0x8000, v196
	s_waitcnt lgkmcnt(1)
	global_store_dwordx4 v197, v[188:191], s[10:11] nt
	s_nop 0
	ds_read_b128 v[188:191], v246 offset:3264
	v_or_b32_e32 v197, 0x10000, v196
	s_waitcnt lgkmcnt(1)
	global_store_dwordx4 v197, v[184:187], s[10:11] nt
	s_nop 0
	ds_read_b128 v[184:187], v246 offset:4352
	v_or_b32_e32 v197, 0x18000, v196
	s_waitcnt lgkmcnt(1)
	global_store_dwordx4 v197, v[188:191], s[10:11] nt
	s_nop 0
	ds_read_b128 v[188:191], v246 offset:5440
	v_or_b32_e32 v197, 0x20000, v196
	s_waitcnt lgkmcnt(1)
	global_store_dwordx4 v197, v[184:187], s[10:11] nt
	s_nop 0
	ds_read_b128 v[184:187], v246 offset:6528
	v_or_b32_e32 v197, 0x28000, v196
	s_waitcnt lgkmcnt(1)
	global_store_dwordx4 v197, v[188:191], s[10:11] nt
	s_nop 0
	ds_read_b128 v[188:191], v246 offset:7616
	v_or_b32_e32 v197, 0x30000, v196
	s_waitcnt lgkmcnt(1)
	global_store_dwordx4 v197, v[184:187], s[10:11] nt
	v_or_b32_e32 v197, 0x38000, v196
	s_waitcnt lgkmcnt(0)
	global_store_dwordx4 v197, v[188:191], s[10:11] nt
